# full grid barriers: the first workgroup of each XCD to arrive issues an early L2 write-back so the XCD leader's write-back on the critical path has less left to flush (skipped on XCD-local barriers)
# speedup vs baseline: 1.0026x; 1.0026x over previous
.Ldvd_19:
	v_add_u32_e32 v6, 1, v5
	v_mad_u64_u32 v[4:5], s[2:3], v4, v3, v[4:5]
	v_cmp_ne_u32_e32 vcc, v6, v4
	s_and_saveexec_b64 s[2:3], vcc
	s_xor_b64 s[2:3], exec, s[2:3]
	v_readlane_b32 s37, v253, 9
	s_cbranch_execz .LBB0_223
	s_waitcnt lgkmcnt(0)
	v_and_b32_e32 v7, 31, v6
	v_cmp_eq_u32_e32 vcc, 1, v7
	s_cbranch_vccz .Lpf_9
	buffer_wbl2 sc1
.Lpf_9:
	v_mov_b32_e32 v2, 0x2000
	global_load_dword v2, v2, s[0:1] offset:1024 sc1
	s_add_u32 s6, s0, 0x2400
	s_addc_u32 s7, s1, 0
	s_waitcnt vmcnt(0)
	v_cmp_eq_u32_e32 vcc, v2, v3
	s_and_saveexec_b64 s[4:5], vcc
	s_cbranch_execz .LBB0_222
	s_mov_b32 s18, 1
	s_mov_b64 s[8:9], 0
	s_branch .LBB0_213

.Ldvd_15:
	v_add_u32_e32 v6, 1, v5
	v_mad_u64_u32 v[4:5], s[2:3], v4, v3, v[4:5]
	v_cmp_ne_u32_e32 vcc, v6, v4
	s_and_saveexec_b64 s[2:3], vcc
	s_xor_b64 s[2:3], exec, s[2:3]
	v_readlane_b32 s37, v253, 9
	s_cbranch_execz .LBB0_454
	s_waitcnt lgkmcnt(0)
	v_and_b32_e32 v7, 31, v6
	v_cmp_eq_u32_e32 vcc, 1, v7
	s_cbranch_vccz .Lpf_7
	v_cmp_eq_u32_e32 vcc, 0, v20
	s_cbranch_vccnz .Lpf_7
	buffer_wbl2 sc1

.Ldvd_7:
	v_add_u32_e32 v6, 1, v5
	v_mad_u64_u32 v[4:5], s[2:3], v4, v3, v[4:5]
	v_cmp_ne_u32_e32 vcc, v6, v4
	s_and_saveexec_b64 s[2:3], vcc
	s_xor_b64 s[2:3], exec, s[2:3]
	s_cbranch_execz .LBB0_766
	s_waitcnt lgkmcnt(0)
	v_and_b32_e32 v7, 31, v6
	v_cmp_eq_u32_e32 vcc, 1, v7
	s_cbranch_vccz .Lpf_3
	buffer_wbl2 sc1

.Ldvd_5:
	v_add_u32_e32 v6, 1, v5
	v_mad_u64_u32 v[4:5], s[2:3], v4, v3, v[4:5]
	v_cmp_ne_u32_e32 vcc, v6, v4
	s_and_saveexec_b64 s[2:3], vcc
	s_xor_b64 s[2:3], exec, s[2:3]
	s_cbranch_execz .LBB0_926
	s_waitcnt lgkmcnt(0)
	v_and_b32_e32 v7, 31, v6
	v_cmp_eq_u32_e32 vcc, 1, v7
	s_cbranch_vccz .Lpf_2
	v_cmp_eq_u32_e32 vcc, 0, v20
	s_cbranch_vccnz .Lpf_2
	buffer_wbl2 sc1
